# baseline (speedup 1.0000x reference)
.Lmy_proj_nosleep:
	v_readfirstlane_b32 s21, v0
	s_cmp_gt_u32 s21, 0x7f
	s_cbranch_scc1 .Lmy_proj_noprio
	s_setprio 2
.Lmy_proj_noprio:
	s_lshr_b32 s20, s21, 6
	s_and_b32 s24, s2, 3
	s_cmp_lg_u32 s24, 0
	s_cselect_b64 s[8:9], -1, 0
	s_cmp_eq_u32 s24, 2
	s_cselect_b32 s3, 28, 40
	s_cselect_b32 s4, 40, 50
	s_cmp_eq_u32 s24, 1
	s_cselect_b32 s3, 18, s3
	s_cselect_b32 s10, 28, s4
	s_cmp_eq_u32 s24, 0
	s_cselect_b64 s[4:5], -1, 0
	s_load_dwordx2 s[16:17], s[0:1], 0x8
	s_and_b64 s[6:7], s[4:5], exec
	s_cselect_b32 s26, 0, s3
	s_cselect_b32 s3, 18, s10
	s_add_i32 s27, s20, s26
	s_cmp_lt_u32 s27, s3
	s_cselect_b64 s[14:15], -1, 0
	s_cmp_ge_u32 s27, s3
	v_and_b32_e32 v146, 63, v0
	s_cbranch_scc1 .LBB2_2
	s_mul_i32 s6, s27, 0x140
	v_or_b32_e32 v2, s6, v146
	v_mov_b32_e32 v3, 0
	s_waitcnt lgkmcnt(0)
	v_lshl_add_u64 v[4:5], v[2:3], 4, s[16:17]
	s_addk_i32 s6, 0x100
	global_load_dwordx4 v[106:109], v[4:5], off
	global_load_dwordx4 v[114:117], v[4:5], off offset:1024
	global_load_dwordx4 v[126:129], v[4:5], off offset:2048
	global_load_dwordx4 v[134:137], v[4:5], off offset:3072
	v_or_b32_e32 v2, s6, v146
	v_lshl_add_u64 v[2:3], v[2:3], 4, s[16:17]
	global_load_dwordx4 v[138:141], v[2:3], off

_Z8k_embed2PKfS0_S0_S0_S0_S0_S0_S0_S0_S0_PDF16_S0_S0_S0_S0_S0_S0_PDv8_DF16_:
	v_readfirstlane_b32 s30, v0
	s_cmpk_gt_u32 s30, 0x7f
	s_cbranch_scc1 .Lmy_e2_noprio
	s_setprio 2
.Lmy_e2_noprio:
	s_cmpk_gt_i32 s2, 0xff
	s_mov_b64 s[4:5], -1
	s_cbranch_scc0 .LBB5_196
	v_lshl_or_b32 v1, s2, 9, v0
	v_add_u32_e32 v2, 0xfffe0000, v1
	s_movk_i32 s3, 0x3e80
	v_cmp_gt_i32_e32 vcc, s3, v2
	s_and_saveexec_b64 s[14:15], vcc
	s_cbranch_execz .LBB5_195
	v_lshrrev_b32_e32 v1, 6, v2
	s_mov_b32 s3, 0x33333334
	v_mul_hi_u32 v3, v1, s3
	v_mul_u32_u24_e32 v3, 5, v3
	s_mov_b32 s3, 0xcccccccd
	v_sub_u32_e32 v3, v1, v3
	v_mul_hi_u32 v1, v2, s3
	v_lshrrev_b32_e32 v1, 4, v1
	v_and_b32_e32 v4, 15, v0
	s_mov_b32 s3, 0xffffff0
	v_and_or_b32 v1, v1, s3, v4
	s_movk_i32 s3, 0x9ff
	v_cmp_lt_u32_e64 s[10:11], s3, v2
	s_movk_i32 s3, 0x167f
	v_cmp_lt_u32_e64 s[8:9], s3, v2
	s_movk_i32 s3, 0x22ff
	s_load_dwordx4 s[24:27], s[0:1], 0x78
	s_load_dwordx8 s[16:23], s[0:1], 0x58
	v_cmp_lt_u32_e64 s[6:7], s3, v2
	s_movk_i32 s3, 0x2f7f
	v_cmp_lt_u32_e64 s[4:5], s3, v2
	s_movk_i32 s3, 0x31ff
	v_cmp_lt_u32_e64 s[12:13], s3, v2
	s_movk_i32 s3, 0xa0
	v_mov_b32_e32 v17, 0
	v_mul_lo_u32 v10, v1, s3
	v_mov_b32_e32 v11, v17
	v_lshlrev_b64 v[14:15], 2, v[10:11]
	v_add_u32_e32 v6, 0xfffe7000, v10
	s_waitcnt lgkmcnt(0)
	v_lshl_add_u64 v[12:13], s[18:19], 0, v[14:15]
	s_mov_b32 s18, 0xfffd3000
	v_ashrrev_i32_e32 v7, 31, v6
	s_mov_b32 s19, -1
	v_lshrrev_b32_e32 v4, 1, v0
	v_lshl_add_u64 v[8:9], v[6:7], 2, s[22:23]
	s_mov_b32 s22, 0xfffba000
	v_lshl_add_u64 v[12:13], v[12:13], 0, s[18:19]
	s_mov_b32 s18, 0xfffec000
	v_and_b32_e32 v4, 24, v4
	v_lshlrev_b32_e32 v16, 5, v1
	v_lshl_add_u64 v[10:11], s[24:25], 0, v[14:15]
	s_mov_b32 s23, -1
	v_lshl_add_u64 v[14:15], s[20:21], 0, v[14:15]
	s_mov_b32 s19, -1
	v_lshl_or_b32 v4, v3, 5, v4
	v_lshl_add_u64 v[6:7], v[16:17], 2, s[26:27]
	v_lshl_add_u64 v[10:11], v[10:11], 0, s[22:23]
	v_lshl_add_u64 v[14:15], v[14:15], 0, s[18:19]
	v_lshlrev_b32_e32 v16, 7, v1
	s_and_saveexec_b64 s[18:19], s[10:11]
	s_xor_b64 s[18:19], exec, s[18:19]
	s_cbranch_execz .LBB5_142
	s_and_saveexec_b64 s[20:21], s[8:9]
	s_xor_b64 s[20:21], exec, s[20:21]
	s_cbranch_execz .LBB5_19
	s_and_saveexec_b64 s[22:23], s[6:7]
	s_xor_b64 s[22:23], exec, s[22:23]
	s_cbranch_execz .LBB5_16
	s_and_saveexec_b64 s[24:25], s[4:5]
	s_xor_b64 s[24:25], exec, s[24:25]
	s_cbranch_execz .LBB5_13
	s_and_saveexec_b64 s[26:27], s[12:13]
	s_xor_b64 s[26:27], exec, s[26:27]
	s_cbranch_execz .LBB5_8
	v_mov_b32_e32 v5, 0
	v_lshl_add_u64 v[18:19], v[4:5], 2, v[8:9]
	global_load_dword v1, v[18:19], off nt
